# grid barrier rounds after the first: all workgroups wait on the cross-XCD arrival counter reaching (round+1)*nXCD; leaders arrive with a non-returning atomic
# speedup vs baseline: 1.0107x; 1.0107x over previous
; __device__ __forceinline__ unsigned xb_ld(unsigned* p)              { return __hip_atomic_load(p, __ATOMIC_RELAXED, __HIP_MEMORY_SCOPE_AGENT); }
; __device__ __forceinline__ unsigned xb_add(unsigned* p, unsigned v) { return __hip_atomic_fetch_add(p, v, __ATOMIC_RELAXED, __HIP_MEMORY_SCOPE_AGENT); }
; #define XB_SPIN(cond, bar) do { unsigned _sp = 0; while (cond) { __builtin_amdgcn_s_sleep(1); \
;     if ((++_sp & 255u) == 0u) { if (xb_ld(&(bar)[XB_TMO])) break; if (_sp > XB_SPIN_CAP) { atomicAdd(&(bar)[XB_TMO], 1u); break; } } } } while (0)
; __device__ __forceinline__ void xcd_barrier(const XcdBarrier& b) {
;     ...
;         unsigned nloc = b.st[0], nx = b.st[1];
;         if (nloc == 0u) { xcd_barrier_complete(bar, b.x, nloc, nx); b.st[0] = nloc; b.st[1] = nx; }
;         const unsigned old = xb_add(&bar[XB_XSUB(b.x)], 1u);
;         const unsigned gen = old / nloc;
;         if (old + 1u == (gen + 1u) * nloc) {
;             __builtin_amdgcn_fence(__ATOMIC_RELEASE, "agent");
;             asm volatile("s_waitcnt vmcnt(0)" ::: "memory");
;             const unsigned og = xb_add(&bar[XB_TOP], 1u);
;             const unsigned tg = og / nx;
;             if (og + 1u == (tg + 1u) * nx) xb_add(&bar[XB_TOPGEN], 1u);
;             else XB_SPIN(xb_ld(&bar[XB_TOPGEN]) == tg, bar);
;             __builtin_amdgcn_fence(__ATOMIC_ACQUIRE, "agent");
;             xb_add(&bar[XB_XGEN(b.x)], 1u);
;             asm volatile("s_waitcnt vmcnt(0)" ::: "memory");
;         } else {
;             XB_SPIN(xb_ld(&bar[XB_XGEN(b.x)]) == gen, bar);
.LBB0_612:
	s_lshl_b32 s2, s2, 6
	s_add_i32 s88, s2, 0x500
	s_lshl_b64 s[6:7], s[88:89], 2
	s_add_u32 s6, s44, s6
	s_addc_u32 s7, s45, s7
	v_mov_b64_e32 v[4:5], s[6:7]
	flat_atomic_add v3, v[4:5], v235 sc0
	buffer_inv sc1
	v_cvt_f32_u32_e32 v4, v2
	v_sub_u32_e32 v5, 0, v2
	v_rcp_iflag_f32_e32 v4, v4
	s_nop 0
	v_mul_f32_e32 v4, 0x4f7ffffe, v4
	v_cvt_u32_f32_e32 v4, v4
	v_mul_lo_u32 v5, v5, v4
	v_mul_hi_u32 v5, v4, v5
	v_add_u32_e32 v4, v4, v5
	s_waitcnt vmcnt(0) lgkmcnt(0)
	v_mul_hi_u32 v4, v3, v4
	v_mul_lo_u32 v5, v4, v2
	v_add_u32_e32 v6, 1, v3
	v_sub_u32_e32 v3, v3, v5
	v_add_u32_e32 v7, 1, v4
	v_sub_u32_e32 v5, v3, v2
	v_cmp_ge_u32_e32 vcc, v3, v2
	s_nop 1
	v_cndmask_b32_e32 v4, v4, v7, vcc
	v_cndmask_b32_e32 v3, v3, v5, vcc
	v_add_u32_e32 v5, 1, v4
	v_cmp_ge_u32_e32 vcc, v3, v2
	s_nop 1
	v_cndmask_b32_e32 v3, v4, v5, vcc
	v_mad_u64_u32 v[4:5], s[6:7], v2, v3, v[2:3]
	v_cmp_ne_u32_e32 vcc, v6, v4
	s_and_saveexec_b64 s[6:7], vcc
	s_xor_b64 s[8:9], exec, s[6:7]
	s_cbranch_execz .LBB0_625
	v_add_u32_e32 v6, 1, v3
	v_mul_lo_u32 v6, v6, v0
	s_add_u32 s12, s44, 0x3400
	s_addc_u32 s13, s45, 0
	v_mov_b64_e32 v[4:5], s[12:13]
	s_mov_b32 s3, 0
.Lgb_spinA0:
	flat_load_dword v0, v[4:5] sc1
	s_waitcnt vmcnt(0) lgkmcnt(0)
	v_sub_u32_e32 v0, v0, v6
	v_cmp_le_i32_e32 vcc, 0, v0
	s_cbranch_vccnz .Lgb_relA0
	s_sleep 1
	s_add_i32 s3, s3, 1
	s_cmp_lt_u32 s3, 0x40000
	s_cbranch_scc1 .Lgb_spinA0

; __device__ __forceinline__ unsigned xb_ld(unsigned* p)              { return __hip_atomic_load(p, __ATOMIC_RELAXED, __HIP_MEMORY_SCOPE_AGENT); }
; __device__ __forceinline__ unsigned xb_add(unsigned* p, unsigned v) { return __hip_atomic_fetch_add(p, v, __ATOMIC_RELAXED, __HIP_MEMORY_SCOPE_AGENT); }
; #define XB_SPIN(cond, bar) do { unsigned _sp = 0; while (cond) { __builtin_amdgcn_s_sleep(1); \
;     if ((++_sp & 255u) == 0u) { if (xb_ld(&(bar)[XB_TMO])) break; if (_sp > XB_SPIN_CAP) { atomicAdd(&(bar)[XB_TMO], 1u); break; } } } } while (0)
; __device__ __forceinline__ void xcd_barrier(const XcdBarrier& b) {
;     ...
;             __builtin_amdgcn_fence(__ATOMIC_RELEASE, "agent");
;             asm volatile("s_waitcnt vmcnt(0)" ::: "memory");
;             const unsigned og = xb_add(&bar[XB_TOP], 1u);
;             const unsigned tg = og / nx;
;             if (og + 1u == (tg + 1u) * nx) xb_add(&bar[XB_TOPGEN], 1u);
;             else XB_SPIN(xb_ld(&bar[XB_TOPGEN]) == tg, bar);
;             __builtin_amdgcn_fence(__ATOMIC_ACQUIRE, "agent");
;             xb_add(&bar[XB_XGEN(b.x)], 1u);
;             asm volatile("s_waitcnt vmcnt(0)" ::: "memory");
;         } else {
;             XB_SPIN(xb_ld(&bar[XB_XGEN(b.x)]) == gen, bar);
.LBB0_625:
	s_andn2_saveexec_b64 s[6:7], s[8:9]
	s_cbranch_execz .LBB0_641
	buffer_wbl2 sc1
	s_waitcnt vmcnt(0)
	v_add_u32_e32 v6, 1, v3
	v_mul_lo_u32 v6, v6, v0
	s_add_u32 s12, s44, 0x3400
	s_addc_u32 s13, s45, 0
	v_mov_b64_e32 v[4:5], s[12:13]
	flat_atomic_add v[4:5], v235
	s_mov_b32 s3, 0

; #define LAS __attribute__((address_space(3)))
; __device__ __forceinline__ float rstd_part16(const float* p, float inv_n) { const f32x4 a = ((const f32x4*)p)[0], b = ((const f32x4*)p)[1], c = ((const f32x4*)p)[2], d = ((const f32x4*)p)[3];
;     const f32x4 s4 = (a + b) + (c + d); return 1.0f / sqrtf(((s4[0] + s4[1]) + (s4[2] + s4[3])) * inv_n + EPS); }
; __device__ __forceinline__ float rstd_part8(const float* p, float inv_n) { const f32x4 a = ((const f32x4*)p)[0], b = ((const f32x4*)p)[1]; const f32x4 s4 = a + b; return 1.0f / sqrtf(((s4[0] + s4[1]) + (s4[2] + s4[3])) * inv_n + EPS); }
; __device__ __forceinline__ float rstd_part4(const float* p, float inv_n) { const f32x4 a = ((const f32x4*)p)[0]; return 1.0f / sqrtf(((a[0] + a[1]) + (a[2] + a[3])) * inv_n + EPS); }
;     EPI_NOMID
;     __device__ __forceinline__ void begin(const Unit& u, int ui, int tid, LAS unsigned char* lds) const { if (tid < 256) rtab_put(lds, ui, tid, rstd_part8(RS + (size_t)(u.pm * 256 + tid) * 8, 1.f / QRANK) * QS_MLA, 0.f); }
.Lgb_relB0:
	s_waitcnt vmcnt(0) lgkmcnt(0)
.LBB0_641:
	s_or_b64 exec, exec, s[42:43]
	v_readlane_b32 s2, v253, 9
	v_readlane_b32 s3, v253, 10
	s_and_b64 vcc, exec, s[2:3]
	s_waitcnt lgkmcnt(0)
	s_barrier
	s_cbranch_vccz .LBB0_694
	v_readlane_b32 s2, v253, 11
	v_readlane_b32 s3, v253, 12
	s_andn2_b64 vcc, exec, s[2:3]
	v_readfirstlane_b32 s3, v188
	s_cbranch_vccnz .LBB0_694
	s_add_u32 s16, s74, 0x600000
	s_movk_i32 s2, 0x100
	s_addc_u32 s17, s75, 0
	v_mov_b32_e32 v2, v188
	v_cmp_gt_i32_e64 s[8:9], s2, v188
	s_and_saveexec_b64 s[12:13], s[8:9]
	s_cbranch_execz .LBB0_645
	v_readlane_b32 s2, v253, 53
	s_nop 1
	v_add_u32_e32 v4, s2, v188
	v_ashrrev_i32_e32 v5, 31, v4
	v_lshlrev_b64 v[4:5], 5, v[4:5]
	v_lshl_add_u64 v[8:9], s[16:17], 0, v[4:5]
	flat_load_dwordx4 v[4:7], v[8:9]
	s_nop 0
	flat_load_dwordx4 v[8:11], v[8:9] offset:16
	s_mov_b32 s2, 0xf800000
	s_waitcnt vmcnt(0) lgkmcnt(0)
	v_pk_add_f32 v[6:7], v[6:7], v[10:11]
	v_pk_add_f32 v[4:5], v[4:5], v[8:9]
	s_nop 0
	v_pk_mov_b32 v[8:9], v[4:5], v[6:7] op_sel:[1,0]
	v_mov_b32_e32 v5, v7
	v_pk_add_f32 v[4:5], v[8:9], v[4:5]
	s_nop 0
	v_add_f32_e32 v0, v4, v5
	v_fmamk_f32 v0, v0, 0x3b2aaaab, v236
	v_mul_f32_e32 v3, 0x4f800000, v0
	v_cmp_gt_f32_e32 vcc, s2, v0
	v_mov_b32_e32 v4, v188
	s_nop 0
	v_cndmask_b32_e32 v0, v0, v3, vcc
	v_sqrt_f32_e32 v3, v0
	v_lshl_add_u32 v4, v4, 3, 0
	v_add_u32_e32 v5, -1, v3
	v_add_u32_e32 v6, 1, v3
	v_fma_f32 v7, -v5, v3, v0
	v_fma_f32 v8, -v6, v3, v0
	v_cmp_ge_f32_e64 s[10:11], 0, v7
	s_nop 1
	v_cndmask_b32_e64 v3, v3, v5, s[10:11]
	v_cmp_lt_f32_e64 s[10:11], 0, v8
	s_nop 1
	v_cndmask_b32_e64 v3, v3, v6, s[10:11]
	v_mul_f32_e32 v5, 0x37800000, v3
	v_cndmask_b32_e32 v3, v3, v5, vcc
	v_cmp_class_f32_e32 vcc, v0, v251
	s_nop 1
	v_cndmask_b32_e32 v0, v3, v0, vcc
	v_div_scale_f32 v3, s[6:7], v0, v0, 1.0
	v_rcp_f32_e32 v5, v3
	v_div_scale_f32 v6, vcc, 1.0, v0, 1.0
	v_fma_f32 v7, -v3, v5, 1.0
	v_fmac_f32_e32 v5, v7, v5
	v_mul_f32_e32 v7, v6, v5
	v_fma_f32 v8, -v3, v7, v6
	v_fmac_f32_e32 v7, v8, v5
	v_fma_f32 v3, -v3, v7, v6
	v_div_fmas_f32 v3, v3, v5, v7
	v_div_fixup_f32 v0, v3, v0, 1.0
	v_mul_f32_e32 v0, 0x3e16c740, v0
	v_add_u32_e32 v3, 0x22400, v4
	ds_write_b64 v3, v[0:1]

; __device__ __forceinline__ unsigned xb_add(unsigned* p, unsigned v) { return __hip_atomic_fetch_add(p, v, __ATOMIC_RELAXED, __HIP_MEMORY_SCOPE_AGENT); }
; __device__ __forceinline__ void xcd_barrier(const XcdBarrier& b) {
;     ...
;         unsigned nloc = b.st[0], nx = b.st[1];
;         if (nloc == 0u) { xcd_barrier_complete(bar, b.x, nloc, nx); b.st[0] = nloc; b.st[1] = nx; }
;         const unsigned old = xb_add(&bar[XB_XSUB(b.x)], 1u);
;         const unsigned gen = old / nloc;
;         if (old + 1u == (gen + 1u) * nloc) {
;             __builtin_amdgcn_fence(__ATOMIC_RELEASE, "agent");
;             asm volatile("s_waitcnt vmcnt(0)" ::: "memory");
;             const unsigned og = xb_add(&bar[XB_TOP], 1u);
.LBB0_734:
	s_lshl_b32 s2, s2, 6
	s_add_i32 s88, s2, 0x500
	s_lshl_b64 s[6:7], s[88:89], 2
	s_add_u32 s6, s44, s6
	s_addc_u32 s7, s45, s7
	v_mov_b64_e32 v[4:5], s[6:7]
	flat_atomic_add v4, v[4:5], v235 sc0
	buffer_inv sc1
	v_cvt_f32_u32_e32 v3, v2
	v_sub_u32_e32 v5, 0, v2
	v_rcp_iflag_f32_e32 v3, v3
	s_nop 0
	v_mul_f32_e32 v3, 0x4f7ffffe, v3
	v_cvt_u32_f32_e32 v3, v3
	v_mul_lo_u32 v5, v5, v3
	v_mul_hi_u32 v5, v3, v5
	v_add_u32_e32 v3, v3, v5
	s_waitcnt vmcnt(0) lgkmcnt(0)
	v_mul_hi_u32 v3, v4, v3
	v_mul_lo_u32 v5, v3, v2
	v_sub_u32_e32 v5, v4, v5
	v_cmp_ge_u32_e32 vcc, v5, v2
	v_add_u32_e32 v6, 1, v3
	s_nop 0
	v_cndmask_b32_e32 v3, v3, v6, vcc
	v_sub_u32_e32 v6, v5, v2
	v_cndmask_b32_e32 v5, v5, v6, vcc
	v_cmp_ge_u32_e32 vcc, v5, v2
	v_add_u32_e32 v5, 1, v3
	v_add_u32_e32 v6, 1, v4
	v_cndmask_b32_e32 v3, v3, v5, vcc
	v_mad_u64_u32 v[4:5], s[6:7], v2, v3, v[2:3]
	v_cmp_ne_u32_e32 vcc, v6, v4
	s_and_saveexec_b64 s[6:7], vcc
	s_xor_b64 s[8:9], exec, s[6:7]
	s_cbranch_execz .LBB0_747
	v_add_u32_e32 v6, 1, v3
	v_mul_lo_u32 v6, v6, v0
	s_add_u32 s12, s44, 0x3400
	s_addc_u32 s13, s45, 0
	v_mov_b64_e32 v[4:5], s[12:13]
	s_mov_b32 s3, 0

; __device__ __forceinline__ unsigned xb_ld(unsigned* p)              { return __hip_atomic_load(p, __ATOMIC_RELAXED, __HIP_MEMORY_SCOPE_AGENT); }
; __device__ __forceinline__ unsigned xb_add(unsigned* p, unsigned v) { return __hip_atomic_fetch_add(p, v, __ATOMIC_RELAXED, __HIP_MEMORY_SCOPE_AGENT); }
; #define XB_SPIN(cond, bar) do { unsigned _sp = 0; while (cond) { __builtin_amdgcn_s_sleep(1); \
;     if ((++_sp & 255u) == 0u) { if (xb_ld(&(bar)[XB_TMO])) break; if (_sp > XB_SPIN_CAP) { atomicAdd(&(bar)[XB_TMO], 1u); break; } } } } while (0)
; __device__ __forceinline__ void xcd_barrier(const XcdBarrier& b) {
;     ...
;             else XB_SPIN(xb_ld(&bar[XB_TOPGEN]) == tg, bar);
;             __builtin_amdgcn_fence(__ATOMIC_ACQUIRE, "agent");
;             xb_add(&bar[XB_XGEN(b.x)], 1u);
;             asm volatile("s_waitcnt vmcnt(0)" ::: "memory");
;         } else {
;             XB_SPIN(xb_ld(&bar[XB_XGEN(b.x)]) == gen, bar);
;             __builtin_amdgcn_fence(__ATOMIC_ACQUIRE, "agent");
;             asm volatile("s_waitcnt vmcnt(0)" ::: "memory");
;         }
;     }
;     __syncthreads();
.Lgb_relB1:
	s_waitcnt vmcnt(0) lgkmcnt(0)
.LBB0_763:
	s_or_b64 exec, exec, s[42:43]
	v_readlane_b32 s2, v253, 61
	v_readlane_b32 s3, v253, 62
	s_andn2_b64 vcc, exec, s[2:3]
	s_mov_b32 s2, 0
	s_waitcnt lgkmcnt(0)
	s_barrier
	s_cbranch_vccnz .LBB0_765
	v_readlane_b32 s2, v254, 11

; #define LAS __attribute__((address_space(3)))
;     __device__ __forceinline__ void begin(const Unit& u, int ui, int tid, LAS unsigned char* lds) const {
;         if (tid < 256) { const float* p = OSS + (size_t)(u.pm * 256 + tid) * 16; const f32x4 a = ((const f32x4*)p)[0], b = ((const f32x4*)p)[1], c = ((const f32x4*)p)[2], d = ((const f32x4*)p)[3];
;             const f32x4 s1 = a + b, s2 = c + d; const float rs = 1.0f / sqrtf(((s1[0] + s1[1]) + (s1[2] + s1[3])) * (1.f / 512.f) + EPS), rm = 1.0f / sqrtf(((s2[0] + s2[1]) + (s2[2] + s2[3])) * (1.f / 512.f) + EPS);
;             ((LAS f32x2*)(lds + OTAB_OFF))[(ui & 1) * 256 + tid] = (f32x2){rs / rm, rm}; }
;     }
.Lgb_relB2:
	s_waitcnt vmcnt(0) lgkmcnt(0)
.LBB0_937:
	s_or_b64 exec, exec, s[42:43]
	v_readlane_b32 s2, v255, 33
	v_readlane_b32 s3, v255, 34
	s_cmp_eq_u32 s2, 0
	v_readlane_b32 s2, v253, 19
	v_readlane_b32 s3, v253, 20
	s_waitcnt lgkmcnt(0)
	s_barrier
	v_cndmask_b32_e64 v0, 0, 1, s[2:3]
	s_cselect_b64 s[44:45], -1, 0
	v_cmp_ne_u32_e64 s[8:9], 1, v0
	s_andn2_b64 vcc, exec, s[2:3]
	v_readfirstlane_b32 s3, v188
	s_cbranch_vccnz .LBB0_976
	s_add_u32 s16, s74, 0x26a00000
	s_movk_i32 s2, 0x100
	s_addc_u32 s17, s75, 0
	v_mov_b32_e32 v0, v188
	v_cmp_gt_i32_e64 s[10:11], s2, v188
	s_and_saveexec_b64 s[14:15], s[10:11]
	s_cbranch_execz .LBB0_940
	v_readlane_b32 s2, v254, 9
	s_nop 1
	v_add_u32_e32 v2, s2, v188
	v_ashrrev_i32_e32 v3, 31, v2
	v_lshlrev_b64 v[2:3], 6, v[2:3]
	v_lshl_add_u64 v[14:15], s[16:17], 0, v[2:3]
	flat_load_dwordx4 v[2:5], v[14:15]
	flat_load_dwordx4 v[6:9], v[14:15] offset:16
	flat_load_dwordx4 v[10:13], v[14:15] offset:32
	s_nop 0
	flat_load_dwordx4 v[14:17], v[14:15] offset:48
	s_mov_b32 s2, 0xf800000
	s_waitcnt vmcnt(0) lgkmcnt(0)
	v_pk_add_f32 v[4:5], v[4:5], v[8:9]
	v_pk_add_f32 v[2:3], v[2:3], v[6:7]
	v_pk_add_f32 v[8:9], v[10:11], v[14:15]
	v_pk_mov_b32 v[10:11], v[2:3], v[4:5] op_sel:[1,0]
	v_mov_b32_e32 v3, v5
	v_pk_add_f32 v[2:3], v[10:11], v[2:3]
	v_pk_add_f32 v[6:7], v[12:13], v[16:17]
	v_add_f32_e32 v2, v2, v3
	v_fmamk_f32 v2, v2, 0x3b000000, v236
	v_cmp_gt_f32_e32 vcc, s2, v2
	v_mul_f32_e32 v3, 0x4f800000, v2
	s_nop 0
	v_cndmask_b32_e32 v2, v2, v3, vcc
	v_sqrt_f32_e32 v3, v2
	s_nop 0
	v_add_u32_e32 v4, -1, v3
	v_fma_f32 v5, -v4, v3, v2
	v_cmp_ge_f32_e64 s[12:13], 0, v5
	v_add_u32_e32 v5, 1, v3
	s_nop 0
	v_cndmask_b32_e64 v4, v3, v4, s[12:13]
	v_fma_f32 v3, -v5, v3, v2
	v_cmp_lt_f32_e64 s[12:13], 0, v3
	s_nop 1
	v_cndmask_b32_e64 v3, v4, v5, s[12:13]
	v_mul_f32_e32 v4, 0x37800000, v3
	v_cndmask_b32_e32 v3, v3, v4, vcc
	v_cmp_class_f32_e32 vcc, v2, v251
	s_nop 1
	v_cndmask_b32_e32 v2, v3, v2, vcc
	v_div_scale_f32 v3, s[6:7], v2, v2, 1.0
	v_rcp_f32_e32 v4, v3
	s_nop 0
	v_fma_f32 v5, -v3, v4, 1.0
	v_fmac_f32_e32 v4, v5, v4
	v_div_scale_f32 v5, vcc, 1.0, v2, 1.0
	v_mul_f32_e32 v10, v5, v4
	v_fma_f32 v11, -v3, v10, v5
	v_fmac_f32_e32 v10, v11, v4
	v_fma_f32 v3, -v3, v10, v5
	v_div_fmas_f32 v3, v3, v4, v10
	v_div_fixup_f32 v4, v3, v2, 1.0
	v_pk_mov_b32 v[2:3], v[8:9], v[6:7] op_sel:[1,0]
	v_mov_b32_e32 v9, v7
	v_pk_add_f32 v[2:3], v[2:3], v[8:9]
	s_nop 0
	v_add_f32_e32 v2, v2, v3
	v_fmamk_f32 v2, v2, 0x3b000000, v236
	v_cmp_gt_f32_e32 vcc, s2, v2
	v_mul_f32_e32 v3, 0x4f800000, v2
	s_nop 0
	v_cndmask_b32_e32 v2, v2, v3, vcc
	v_sqrt_f32_e32 v3, v2
	s_nop 0
	v_add_u32_e32 v5, -1, v3
	v_fma_f32 v6, -v5, v3, v2
	v_cmp_ge_f32_e64 s[12:13], 0, v6
	v_add_u32_e32 v6, 1, v3
	s_nop 0
	v_cndmask_b32_e64 v5, v3, v5, s[12:13]
	v_fma_f32 v3, -v6, v3, v2
	v_cmp_lt_f32_e64 s[12:13], 0, v3
	s_nop 1
	v_cndmask_b32_e64 v3, v5, v6, s[12:13]
	v_mul_f32_e32 v5, 0x37800000, v3
	v_cndmask_b32_e32 v3, v3, v5, vcc
	v_cmp_class_f32_e32 vcc, v2, v251
	s_nop 1
	v_cndmask_b32_e32 v2, v3, v2, vcc
	v_div_scale_f32 v3, s[6:7], v2, v2, 1.0
	v_rcp_f32_e32 v5, v3
	s_nop 0
	v_fma_f32 v6, -v3, v5, 1.0
	v_fmac_f32_e32 v5, v6, v5
	v_div_scale_f32 v6, vcc, 1.0, v2, 1.0
	v_mul_f32_e32 v7, v6, v5
	v_fma_f32 v8, -v3, v7, v6
	v_fmac_f32_e32 v7, v8, v5
	v_fma_f32 v3, -v3, v7, v6
	v_div_fmas_f32 v3, v3, v5, v7
	v_div_fixup_f32 v3, v3, v2, 1.0
	v_div_scale_f32 v2, s[6:7], v3, v3, v4
	v_rcp_f32_e32 v5, v2
	s_nop 0
	v_fma_f32 v6, -v2, v5, 1.0
	v_fmac_f32_e32 v5, v6, v5
	v_div_scale_f32 v6, vcc, v4, v3, v4
	v_mul_f32_e32 v7, v6, v5
	v_fma_f32 v8, -v2, v7, v6
	v_fmac_f32_e32 v7, v8, v5
	v_fma_f32 v2, -v2, v7, v6
	v_div_fmas_f32 v2, v2, v5, v7
	v_div_fixup_f32 v2, v2, v3, v4
	v_lshl_add_u32 v4, v188, 3, 0
	v_add_u32_e32 v4, 0x22400, v4
	ds_write_b64 v4, v[2:3]

; __device__ __forceinline__ unsigned xb_add(unsigned* p, unsigned v) { return __hip_atomic_fetch_add(p, v, __ATOMIC_RELAXED, __HIP_MEMORY_SCOPE_AGENT); }
; __device__ __forceinline__ void xcd_barrier(const XcdBarrier& b) {
;     ...
;         unsigned nloc = b.st[0], nx = b.st[1];
;         if (nloc == 0u) { xcd_barrier_complete(bar, b.x, nloc, nx); b.st[0] = nloc; b.st[1] = nx; }
;         const unsigned old = xb_add(&bar[XB_XSUB(b.x)], 1u);
;         const unsigned gen = old / nloc;
;         if (old + 1u == (gen + 1u) * nloc) {
;             __builtin_amdgcn_fence(__ATOMIC_RELEASE, "agent");
;             asm volatile("s_waitcnt vmcnt(0)" ::: "memory");
;             const unsigned og = xb_add(&bar[XB_TOP], 1u);
.LBB0_991:
	s_lshl_b32 s2, s2, 6
	s_add_i32 s88, s2, 0x500
	s_lshl_b64 s[6:7], s[88:89], 2
	s_add_u32 s6, s48, s6
	s_addc_u32 s7, s49, s7
	v_mov_b64_e32 v[4:5], s[6:7]
	flat_atomic_add v4, v[4:5], v235 sc0
	buffer_inv sc1
	v_cvt_f32_u32_e32 v3, v2
	v_sub_u32_e32 v5, 0, v2
	v_rcp_iflag_f32_e32 v3, v3
	s_nop 0
	v_mul_f32_e32 v3, 0x4f7ffffe, v3
	v_cvt_u32_f32_e32 v3, v3
	v_mul_lo_u32 v5, v5, v3
	v_mul_hi_u32 v5, v3, v5
	v_add_u32_e32 v3, v3, v5
	s_waitcnt vmcnt(0) lgkmcnt(0)
	v_mul_hi_u32 v3, v4, v3
	v_mul_lo_u32 v5, v3, v2
	v_sub_u32_e32 v5, v4, v5
	v_cmp_ge_u32_e32 vcc, v5, v2
	v_add_u32_e32 v6, 1, v3
	s_nop 0
	v_cndmask_b32_e32 v3, v3, v6, vcc
	v_sub_u32_e32 v6, v5, v2
	v_cndmask_b32_e32 v5, v5, v6, vcc
	v_cmp_ge_u32_e32 vcc, v5, v2
	v_add_u32_e32 v5, 1, v3
	v_add_u32_e32 v6, 1, v4
	v_cndmask_b32_e32 v3, v3, v5, vcc
	v_mad_u64_u32 v[4:5], s[6:7], v2, v3, v[2:3]
	v_cmp_ne_u32_e32 vcc, v6, v4
	s_and_saveexec_b64 s[6:7], vcc
	s_xor_b64 s[10:11], exec, s[6:7]
	s_cbranch_execz .LBB0_1004
	v_add_u32_e32 v6, 1, v3
	v_mul_lo_u32 v6, v6, v0
	s_add_u32 s12, s48, 0x3400
	s_addc_u32 s13, s49, 0
	v_mov_b64_e32 v[4:5], s[12:13]
	s_mov_b32 s3, 0

; __device__ __forceinline__ unsigned xb_ld(unsigned* p)              { return __hip_atomic_load(p, __ATOMIC_RELAXED, __HIP_MEMORY_SCOPE_AGENT); }
; __device__ __forceinline__ unsigned xb_add(unsigned* p, unsigned v) { return __hip_atomic_fetch_add(p, v, __ATOMIC_RELAXED, __HIP_MEMORY_SCOPE_AGENT); }
; #define XB_SPIN(cond, bar) do { unsigned _sp = 0; while (cond) { __builtin_amdgcn_s_sleep(1); \
;     if ((++_sp & 255u) == 0u) { if (xb_ld(&(bar)[XB_TMO])) break; if (_sp > XB_SPIN_CAP) { atomicAdd(&(bar)[XB_TMO], 1u); break; } } } } while (0)
; __device__ __forceinline__ void xcd_barrier(const XcdBarrier& b) {
;     ...
;             __builtin_amdgcn_fence(__ATOMIC_RELEASE, "agent");
;             asm volatile("s_waitcnt vmcnt(0)" ::: "memory");
;             const unsigned og = xb_add(&bar[XB_TOP], 1u);
;             const unsigned tg = og / nx;
;             if (og + 1u == (tg + 1u) * nx) xb_add(&bar[XB_TOPGEN], 1u);
;             else XB_SPIN(xb_ld(&bar[XB_TOPGEN]) == tg, bar);
;             __builtin_amdgcn_fence(__ATOMIC_ACQUIRE, "agent");
;             xb_add(&bar[XB_XGEN(b.x)], 1u);
;             asm volatile("s_waitcnt vmcnt(0)" ::: "memory");
;         } else {
;             XB_SPIN(xb_ld(&bar[XB_XGEN(b.x)]) == gen, bar);
.LBB0_1004:
	s_andn2_saveexec_b64 s[6:7], s[10:11]
	s_cbranch_execz .LBB0_1020
	buffer_wbl2 sc1
	s_waitcnt vmcnt(0)
	v_add_u32_e32 v6, 1, v3
	v_mul_lo_u32 v6, v6, v0
	s_add_u32 s12, s48, 0x3400
	s_addc_u32 s13, s49, 0
	v_mov_b64_e32 v[4:5], s[12:13]
	flat_atomic_add v[4:5], v235
	s_mov_b32 s3, 0

; #define LAS __attribute__((address_space(3)))
; template <class Tp> __device__ __forceinline__ Tp* wsp(const Frame& F, size_t off) { return (Tp*)(F.ws + off); }
; __device__ __forceinline__ void phase_route(Frame& F, int l, bool dummy = false) {
;     ...
;     const char* WRT = (const char*)(F.ws + WS_WR) + (size_t)l * 2 * RT_STRIDE;
;     const bf16_t* HB = wsp<bf16_t>(F, WS_HB); float* RS = wsp<float>(F, WS_RS);
;     unsigned* cnt = wsp<unsigned>(F, WS_CTL) + CW_CNT + 64 * 32 * (dummy ? NLAYER + l : l); int* liste = dummy ? wsp<int>(F, WS_Y) : wsp<int>(F, WS_LISTE); float* listw = dummy ? wsp<float>(F, WS_Y + 4 * MiB) : wsp<float>(F, WS_LISTW);
;     const float* brg = P.in[14] + l * 4; const float* bre = P.in[16] + l * 32;
;     constexpr int SC_OFF = RT_STRIDE, SC_WAVE = 16 * 49 * 4, RK_OFF = SC_OFF + NWAVES * SC_WAVE;
;     LAS unsigned* lcnt = (LAS unsigned*)(F.lds + RK_OFF); LAS unsigned* lbase = lcnt + 32; LAS unsigned* ent = lcnt + 64;
;     LAS float* sc = (LAS float*)(F.lds + SC_OFF + F.wave * SC_WAVE);
;     const int step = F.ngw(), ri = F.lane & 15, kq = F.lane >> 4;
;     for (int pc = F.wave; pc < 73; pc += NWAVES) lds_dma16(WRT + (size_t)pc * 1024 + F.lane * 16, F.lds + pc * 1024);
.Lgb_relB3:
	s_waitcnt vmcnt(0) lgkmcnt(0)
.LBB0_1020:
	s_or_b64 exec, exec, s[46:47]
	s_waitcnt lgkmcnt(0)
	s_barrier
	v_cndmask_b32_e64 v0, 0, 1, s[94:95]
	v_and_b32_e32 v156, 63, v188
	v_cmp_ne_u32_e64 s[10:11], 1, v0
	s_andn2_b64 vcc, exec, s[94:95]
	v_lshlrev_b32_e32 v0, 4, v156
	s_cbranch_vccnz .LBB0_1023
	v_readlane_b32 s2, v254, 18
	s_add_u32 s2, s74, s2
	v_readlane_b32 s3, v254, 19
	s_addc_u32 s3, s75, s3
	s_nop 0
	v_lshl_add_u64 v[2:3], s[2:3], 0, v[0:1]
	s_mov_b32 s2, s58
	s_mov_b32 s3, s55

; #define LAS __attribute__((address_space(3)))
; template <class Tp> __device__ __forceinline__ Tp* wsp(const Frame& F, size_t off) { return (Tp*)(F.ws + off); }
; __device__ __forceinline__ void moe_table(Frame& F, int l) {
;     LAS int* tb = (LAS int*)(F.lds + pg8::STAGE_BYTES);
;     __syncthreads();
;     if (F.tid < NEXP) { const unsigned* cnt = wsp<unsigned>(F, WS_CTL) + CW_CNT + 64 * 32 * l;
;         const int c = (int)__hip_atomic_load(cnt + 64 * F.tid, __ATOMIC_RELAXED, __HIP_MEMORY_SCOPE_AGENT); tb[40 + F.tid] = c; tb[80 + F.tid] = (c + 255) >> 8; }
;     __syncthreads();
;     if (F.tid <= NEXP) { int acc = 0; for (int e = 0; e < F.tid; ++e) acc += tb[80 + e]; tb[F.tid] = acc; }
.Lgb_relB4:
	s_waitcnt vmcnt(0) lgkmcnt(0)
.LBB0_1096:
	s_or_b64 exec, exec, s[44:45]
	s_waitcnt lgkmcnt(0)
	s_barrier
	s_nop 0
	v_cmp_gt_i32_e32 vcc, 32, v188
	v_lshlrev_b32_e32 v6, 6, v188
	s_barrier
	s_and_saveexec_b64 s[10:11], vcc
	s_cbranch_execz .LBB0_1098
	s_add_u32 s2, s74, s46
	s_addc_u32 s3, s75, s47
	v_ashrrev_i32_e32 v7, 31, v6
	v_lshl_add_u64 v[2:3], v[6:7], 2, s[2:3]
	v_add_co_u32_e32 v2, vcc, 0x8000, v2
	s_add_i32 s2, 0, 0x20000
	s_nop 0
	v_addc_co_u32_e32 v3, vcc, 0, v3, vcc
	flat_load_dword v0, v[2:3] sc1
	v_lshl_add_u32 v2, v188, 2, s2
	s_waitcnt vmcnt(0) lgkmcnt(0)
	v_add_u32_e32 v3, 0xff, v0
	v_ashrrev_i32_e32 v3, 8, v3
	ds_write2_b32 v2, v0, v3 offset0:40 offset1:80

; __device__ __forceinline__ unsigned xb_add(unsigned* p, unsigned v) { return __hip_atomic_fetch_add(p, v, __ATOMIC_RELAXED, __HIP_MEMORY_SCOPE_AGENT); }
; __device__ __forceinline__ void xcd_barrier(const XcdBarrier& b) {
;     ...
;         unsigned nloc = b.st[0], nx = b.st[1];
;         if (nloc == 0u) { xcd_barrier_complete(bar, b.x, nloc, nx); b.st[0] = nloc; b.st[1] = nx; }
;         const unsigned old = xb_add(&bar[XB_XSUB(b.x)], 1u);
;         const unsigned gen = old / nloc;
;         if (old + 1u == (gen + 1u) * nloc) {
;             __builtin_amdgcn_fence(__ATOMIC_RELEASE, "agent");
;             asm volatile("s_waitcnt vmcnt(0)" ::: "memory");
;             const unsigned og = xb_add(&bar[XB_TOP], 1u);
.LBB0_1272:
	s_lshl_b32 s2, s2, 6
	s_add_i32 s88, s2, 0x500
	s_lshl_b64 s[6:7], s[88:89], 2
	s_add_u32 s6, s46, s6
	s_addc_u32 s7, s47, s7
	v_mov_b64_e32 v[4:5], s[6:7]
	flat_atomic_add v4, v[4:5], v235 sc0
	buffer_inv sc1
	v_cvt_f32_u32_e32 v3, v2
	v_sub_u32_e32 v5, 0, v2
	v_rcp_iflag_f32_e32 v3, v3
	s_nop 0
	v_mul_f32_e32 v3, 0x4f7ffffe, v3
	v_cvt_u32_f32_e32 v3, v3
	v_mul_lo_u32 v5, v5, v3
	v_mul_hi_u32 v5, v3, v5
	v_add_u32_e32 v3, v3, v5
	s_waitcnt vmcnt(0) lgkmcnt(0)
	v_mul_hi_u32 v3, v4, v3
	v_mul_lo_u32 v5, v3, v2
	v_sub_u32_e32 v5, v4, v5
	v_cmp_ge_u32_e32 vcc, v5, v2
	v_add_u32_e32 v6, 1, v3
	s_nop 0
	v_cndmask_b32_e32 v3, v3, v6, vcc
	v_sub_u32_e32 v6, v5, v2
	v_cndmask_b32_e32 v5, v5, v6, vcc
	v_cmp_ge_u32_e32 vcc, v5, v2
	v_add_u32_e32 v5, 1, v3
	v_add_u32_e32 v6, 1, v4
	v_cndmask_b32_e32 v3, v3, v5, vcc
	v_mad_u64_u32 v[4:5], s[6:7], v2, v3, v[2:3]
	v_cmp_ne_u32_e32 vcc, v6, v4
	s_and_saveexec_b64 s[6:7], vcc
	s_xor_b64 s[10:11], exec, s[6:7]
	s_cbranch_execz .LBB0_1285
	v_add_u32_e32 v6, 1, v3
	v_mul_lo_u32 v6, v6, v0
	s_add_u32 s12, s46, 0x3400
	s_addc_u32 s13, s47, 0
	v_mov_b64_e32 v[4:5], s[12:13]
	s_mov_b32 s3, 0

; __device__ __forceinline__ unsigned xb_ld(unsigned* p)              { return __hip_atomic_load(p, __ATOMIC_RELAXED, __HIP_MEMORY_SCOPE_AGENT); }
; __device__ __forceinline__ unsigned xb_add(unsigned* p, unsigned v) { return __hip_atomic_fetch_add(p, v, __ATOMIC_RELAXED, __HIP_MEMORY_SCOPE_AGENT); }
; #define XB_SPIN(cond, bar) do { unsigned _sp = 0; while (cond) { __builtin_amdgcn_s_sleep(1); \
;     if ((++_sp & 255u) == 0u) { if (xb_ld(&(bar)[XB_TMO])) break; if (_sp > XB_SPIN_CAP) { atomicAdd(&(bar)[XB_TMO], 1u); break; } } } } while (0)
; __device__ __forceinline__ void xcd_barrier(const XcdBarrier& b) {
;     ...
;             __builtin_amdgcn_fence(__ATOMIC_RELEASE, "agent");
;             asm volatile("s_waitcnt vmcnt(0)" ::: "memory");
;             const unsigned og = xb_add(&bar[XB_TOP], 1u);
;             const unsigned tg = og / nx;
;             if (og + 1u == (tg + 1u) * nx) xb_add(&bar[XB_TOPGEN], 1u);
;             else XB_SPIN(xb_ld(&bar[XB_TOPGEN]) == tg, bar);
;             __builtin_amdgcn_fence(__ATOMIC_ACQUIRE, "agent");
;             xb_add(&bar[XB_XGEN(b.x)], 1u);
;             asm volatile("s_waitcnt vmcnt(0)" ::: "memory");
;         } else {
;             XB_SPIN(xb_ld(&bar[XB_XGEN(b.x)]) == gen, bar);
.LBB0_1285:
	s_andn2_saveexec_b64 s[6:7], s[10:11]
	s_cbranch_execz .LBB0_1301
	buffer_wbl2 sc1
	s_waitcnt vmcnt(0)
	v_add_u32_e32 v6, 1, v3
	v_mul_lo_u32 v6, v6, v0
	s_add_u32 s12, s46, 0x3400
	s_addc_u32 s13, s47, 0
	v_mov_b64_e32 v[4:5], s[12:13]
	flat_atomic_add v[4:5], v235
	s_mov_b32 s3, 0

;     __device__ __forceinline__ bool next(int i, Unit& u) const { return o.next(i, u); }
;     __device__ __forceinline__ bool next(int i, Unit& u) const {
;         if ((G & 7) == 0) {
;             const int x = c & 7, W = G >> 3, q = i * W + (c >> 3);
;             int tq = q / npn; u.pn = q % npn;
; #pragma unroll 1
;             for (int k = 0; k < 4; ++k) { const int e = x + 8 * k, nte = tb[e + 1] - tb[e];
;                 if (tq < nte) { u.e = e; u.tile = tq; u.pm = tb[e] + tq; const int rem = tb[40 + e] - 256 * tq; u.nrows = rem < 256 ? rem : 256; return true; }
;                 tq -= nte; }
;             return false;
.Lgb_relB5:
	s_waitcnt vmcnt(0) lgkmcnt(0)
.LBB0_1301:
	s_or_b64 exec, exec, s[44:45]
	s_waitcnt lgkmcnt(0)
	s_barrier
	s_and_b64 vcc, exec, s[90:91]
	v_readfirstlane_b32 s26, v188
	s_cbranch_vccz .LBB0_1307
	v_readlane_b32 s2, v255, 4
	s_mov_b64 s[14:15], 0
	s_nop 0
	v_mov_b32_e32 v0, s2
	ds_read_b32 v0, v0
	s_waitcnt lgkmcnt(0)
	v_lshlrev_b32_e32 v0, 2, v0
	v_cmp_ge_i32_e32 vcc, s77, v0
	s_cbranch_vccnz .LBB0_1308
	s_add_i32 s2, 0, 0x20004
	s_mov_b32 s3, 0
	s_branch .LBB0_1305

; template <class Tp> __device__ __forceinline__ Tp* wsp(const Frame& F, size_t off) { return (Tp*)(F.ws + off); }
; __device__ __forceinline__ void phase_norm2(Frame& F, int l, float ysc) {
;     bf16_t* HB = wsp<bf16_t>(F, WS_HB); float* RS = wsp<float>(F, WS_RS); const bf16_t* Y = wsp<bf16_t>(F, WS_Y);
;     for (int row0 = 2 * F.gw(); row0 < T; row0 += 2 * F.ngw()) {
;         u32x4 hw[2][2], ya[2][2], yb[2][2];
; #pragma unroll
;         for (int q = 0; q < 2; ++q) { const u32x4* xr = (const u32x4*)(HB + (size_t)(row0 + q) * DM) + F.lane; const u32x4* y0 = (const u32x4*)(Y + (size_t)(row0 + q) * 2 * DM) + F.lane; const u32x4* y1 = y0 + DM / 8;
.Lgb_relB6:
	s_waitcnt vmcnt(0) lgkmcnt(0)
.LBB0_1418:
	s_or_b64 exec, exec, s[44:45]
	v_readlane_b32 s2, v253, 4
	v_readlane_b32 s3, v253, 5
	s_andn2_b64 vcc, exec, s[2:3]
	s_waitcnt lgkmcnt(0)
	s_barrier
	s_cbranch_vccnz .LBB0_1425
	v_and_b32_e32 v0, 63, v188
	v_readlane_b32 s2, v254, 39
	v_cmp_eq_u32_e64 s[10:11], 0, v0
	v_lshlrev_b32_e32 v0, 4, v0
	v_readlane_b32 s3, v254, 40
	v_readlane_b32 s14, v254, 35
	v_readlane_b32 s15, v254, 36
	v_lshl_add_u64 v[38:39], s[2:3], 0, v[0:1]
	v_readlane_b32 s2, v254, 45
	v_readlane_b32 s3, v254, 46
	s_nop 1
	v_lshl_add_u64 v[40:41], s[2:3], 0, v[0:1]
	v_readlane_b32 s2, v254, 43
	v_readlane_b32 s3, v254, 44
	s_branch .LBB0_1421

; __device__ __forceinline__ u32x4 pack8(f32x4 a, f32x4 b) { u32x4 w; w.x = pk2(a[0], a[1]); w.y = pk2(a[2], a[3]); w.z = pk2(b[0], b[1]); w.w = pk2(b[2], b[3]); return w; }
; template <class Tp> __device__ __forceinline__ Tp* wsp(const Frame& F, size_t off) { return (Tp*)(F.ws + off); }
; __device__ __forceinline__ void phase_pconv(Frame& F, int l) {
;     const Params& P = *F.P; bf16_t* PB = wsp<bf16_t>(F, WS_PB); const float* pl = P.in[1] + (size_t)l * T * DPLE;
;     for (int i = F.bx * NTHREADS + F.tid; i < T * DPLE / 16; i += F.G * NTHREADS) {
;         const f32x4* pp = (const f32x4*)(pl + (size_t)i * 16); const f32x4 a = pp[0], b2 = pp[1], c2 = pp[2], d2 = pp[3];
;         u32x4* dst = (u32x4*)(PB + (size_t)i * 16); dst[0] = pack8(a, b2); dst[1] = pack8(c2, d2); }
; }
.Lgb_relB7:
	s_waitcnt vmcnt(0) lgkmcnt(0)
.LBB0_1469:
	s_or_b64 exec, exec, s[44:45]
	s_cmp_eq_u32 s62, 3
	s_waitcnt lgkmcnt(0)
	s_barrier
	s_cbranch_scc1 .LBB0_1474
	v_readlane_b32 s2, v253, 3
	s_nop 1
	v_add_u32_e32 v2, s2, v188
	s_mov_b32 s2, 0x80000
	v_cmp_gt_i32_e32 vcc, s2, v2
	s_and_saveexec_b64 s[10:11], vcc
	v_readlane_b32 s16, v255, 28
	v_readlane_b32 s18, v255, 30
	v_readlane_b32 s6, v255, 26
	v_readlane_b32 s17, v255, 29
	v_readlane_b32 s19, v255, 31
	v_readlane_b32 s7, v255, 27
	s_cbranch_execz .LBB0_1473
	v_ashrrev_i32_e32 v3, 31, v2
	v_lshlrev_b64 v[6:7], 5, v[2:3]
	v_lshl_add_u64 v[6:7], s[74:75], 0, v[6:7]
	s_mov_b64 s[2:3], 0x2ac00010
	v_readlane_b32 s14, v254, 51
	v_lshlrev_b64 v[4:5], 6, v[2:3]
	v_lshl_add_u64 v[6:7], v[6:7], 0, s[2:3]
	s_mov_b64 s[12:13], 0
	v_readlane_b32 s15, v254, 52
	s_cmp_lg_u32 s6, 0x20000
	s_cbranch_scc1 .LBB0_1472
	v_lshl_add_u64 v[20:21], s[14:15], 0, v[4:5]
	global_load_dwordx4 v[24:27], v[20:21], off
	global_load_dwordx4 v[28:31], v[20:21], off offset:16
	global_load_dwordx4 v[32:35], v[20:21], off offset:32
	global_load_dwordx4 v[36:39], v[20:21], off offset:48
	s_add_u32 s14, s14, s16
	s_addc_u32 s15, s15, s17
	v_lshl_add_u64 v[20:21], s[14:15], 0, v[4:5]
	global_load_dwordx4 v[40:43], v[20:21], off
	global_load_dwordx4 v[44:47], v[20:21], off offset:16
	global_load_dwordx4 v[48:51], v[20:21], off offset:32
	global_load_dwordx4 v[52:55], v[20:21], off offset:48
	s_add_u32 s14, s14, s16
	s_addc_u32 s15, s15, s17
	v_lshl_add_u64 v[20:21], s[14:15], 0, v[4:5]
	global_load_dwordx4 v[56:59], v[20:21], off
	global_load_dwordx4 v[60:63], v[20:21], off offset:16
	global_load_dwordx4 v[64:67], v[20:21], off offset:32
	global_load_dwordx4 v[68:71], v[20:21], off offset:48
	s_add_u32 s14, s14, s16
	s_addc_u32 s15, s15, s17
	v_lshl_add_u64 v[20:21], s[14:15], 0, v[4:5]
	global_load_dwordx4 v[72:75], v[20:21], off
	global_load_dwordx4 v[76:79], v[20:21], off offset:16
	global_load_dwordx4 v[80:83], v[20:21], off offset:32
	global_load_dwordx4 v[84:87], v[20:21], off offset:48
	s_add_u32 s14, s14, s16
	s_addc_u32 s15, s15, s17
	s_waitcnt vmcnt(12)
	v_cvt_pk_bf16_f32 v8, v24, v25
	v_cvt_pk_bf16_f32 v9, v26, v27
	v_cvt_pk_bf16_f32 v10, v28, v29
	v_cvt_pk_bf16_f32 v11, v30, v31
	v_cvt_pk_bf16_f32 v12, v32, v33
	v_cvt_pk_bf16_f32 v13, v34, v35
	v_cvt_pk_bf16_f32 v14, v36, v37
	v_cvt_pk_bf16_f32 v15, v38, v39
	global_store_dwordx4 v[6:7], v[8:11], off offset:-16
	global_store_dwordx4 v[6:7], v[12:15], off
	s_nop 1
	v_lshl_add_u64 v[6:7], v[6:7], 0, s[18:19]
	s_waitcnt vmcnt(10)
	v_cvt_pk_bf16_f32 v8, v40, v41
	v_cvt_pk_bf16_f32 v9, v42, v43
	v_cvt_pk_bf16_f32 v10, v44, v45
	v_cvt_pk_bf16_f32 v11, v46, v47
	v_cvt_pk_bf16_f32 v12, v48, v49
	v_cvt_pk_bf16_f32 v13, v50, v51
	v_cvt_pk_bf16_f32 v14, v52, v53
	v_cvt_pk_bf16_f32 v15, v54, v55
	global_store_dwordx4 v[6:7], v[8:11], off offset:-16
	global_store_dwordx4 v[6:7], v[12:15], off
	s_nop 1
	v_lshl_add_u64 v[6:7], v[6:7], 0, s[18:19]
	s_waitcnt vmcnt(8)
	v_cvt_pk_bf16_f32 v8, v56, v57
	v_cvt_pk_bf16_f32 v9, v58, v59
	v_cvt_pk_bf16_f32 v10, v60, v61
	v_cvt_pk_bf16_f32 v11, v62, v63
	v_cvt_pk_bf16_f32 v12, v64, v65
	v_cvt_pk_bf16_f32 v13, v66, v67
	v_cvt_pk_bf16_f32 v14, v68, v69
	v_cvt_pk_bf16_f32 v15, v70, v71
	global_store_dwordx4 v[6:7], v[8:11], off offset:-16
	global_store_dwordx4 v[6:7], v[12:15], off
	s_nop 1
	v_lshl_add_u64 v[6:7], v[6:7], 0, s[18:19]
	s_waitcnt vmcnt(6)
	v_cvt_pk_bf16_f32 v8, v72, v73
	v_cvt_pk_bf16_f32 v9, v74, v75
	v_cvt_pk_bf16_f32 v10, v76, v77
	v_cvt_pk_bf16_f32 v11, v78, v79
	v_cvt_pk_bf16_f32 v12, v80, v81
	v_cvt_pk_bf16_f32 v13, v82, v83
	v_cvt_pk_bf16_f32 v14, v84, v85
	v_cvt_pk_bf16_f32 v15, v86, v87
	global_store_dwordx4 v[6:7], v[8:11], off offset:-16
	global_store_dwordx4 v[6:7], v[12:15], off
	s_nop 1
	v_lshl_add_u64 v[6:7], v[6:7], 0, s[18:19]
	s_branch .LBB0_1473

; __device__ __forceinline__ unsigned xb_ld(unsigned* p)              { return __hip_atomic_load(p, __ATOMIC_RELAXED, __HIP_MEMORY_SCOPE_AGENT); }
; __device__ __forceinline__ unsigned xb_add(unsigned* p, unsigned v) { return __hip_atomic_fetch_add(p, v, __ATOMIC_RELAXED, __HIP_MEMORY_SCOPE_AGENT); }
; #define XB_SPIN(cond, bar) do { unsigned _sp = 0; while (cond) { __builtin_amdgcn_s_sleep(1); \
;     if ((++_sp & 255u) == 0u) { if (xb_ld(&(bar)[XB_TMO])) break; if (_sp > XB_SPIN_CAP) { atomicAdd(&(bar)[XB_TMO], 1u); break; } } } } while (0)
; __device__ __forceinline__ void xcd_barrier(const XcdBarrier& b) {
;     ...
;             else XB_SPIN(xb_ld(&bar[XB_TOPGEN]) == tg, bar);
;             __builtin_amdgcn_fence(__ATOMIC_ACQUIRE, "agent");
;             xb_add(&bar[XB_XGEN(b.x)], 1u);
;             asm volatile("s_waitcnt vmcnt(0)" ::: "memory");
;         } else {
;             XB_SPIN(xb_ld(&bar[XB_XGEN(b.x)]) == gen, bar);
;             __builtin_amdgcn_fence(__ATOMIC_ACQUIRE, "agent");
;             asm volatile("s_waitcnt vmcnt(0)" ::: "memory");
;         }
;     }
;     __syncthreads();
.Lgb_skip9:
	s_getpc_b64 s[98:99]
